# router phase: the next row's loads are requested right after the current row's registers are consumed (one row of prefetch)
# baseline (speedup 1.0000x reference)
; #define GAS __attribute__((address_space(1)))
; __device__ __forceinline__ f32x4 bf4_to_f32(u32x2_g a) { return (f32x4){__uint_as_float(a.x << 16), __uint_as_float(a.x & 0xffff0000u), __uint_as_float(a.y << 16), __uint_as_float(a.y & 0xffff0000u)}; }
; #define lane (lane_id())
; __device__ __forceinline__ void router_phase(const Ptrs& P, const float* gain, LAS unsigned char* lds, int vcu, int G, int tid, int wave, int lane) {
;     ...
;     int gw = vcu * NWAVES + wave; asm volatile("" : "+s"(gw));
;     const int NGW = G * NWAVES;
;     int li = wave;
;     for (int m = gw; m < M; m += NGW, li += NWAVES) {
;         const GAS u32x2_g* xr = (const GAS u32x2_g*)(P.H + (size_t)m * D) + lane;
;         f32x4 v[8]; float s = 0.f;
; #pragma unroll
;         for (int j = 0; j < 8; ++j) { v[j] = bf4_to_f32(xr[64 * j]); s += (v[j].x * v[j].x + v[j].y * v[j].y) + (v[j].z * v[j].z + v[j].w * v[j].w); }
;         const float r = 1.0f / sqrtf(wave_sum(s) * (1.0f / D) + EPS);
;         float lg[8];
; #pragma unroll
;         for (int e = 0; e < 8; ++e) lg[e] = 0.f;
;         GAS unsigned* o4 = (GAS unsigned*)(P.AB8 + (size_t)m * D) + lane;
; #pragma unroll
;         for (int j = 0; j < 8; ++j) { const f32x4 g = ((const GAS f32x4*)gain)[lane + 64 * j];
.LBB0_1472:
	s_mov_b64 s[26:27], 0x2000
	s_or_b64 exec, exec, s[18:19]
	s_waitcnt lgkmcnt(0)
	v_readlane_b32 s22, v253, 50
	s_waitcnt lgkmcnt(0)
	s_barrier
	s_cmpk_lt_i32 s22, 0x2000
	s_cselect_b64 s[24:25], -1, 0
	s_cmpk_gt_i32 s22, 0x1fff
	v_cmp_eq_u32_e64 s[38:39], 0, v34
	v_readlane_b32 s23, v253, 51
	s_cbranch_scc1 .LBB0_1477
	v_ashrrev_i32_e32 v35, 31, v34
	v_lshl_add_u64 v[2:3], v[34:35], 4, s[20:21]
	v_lshl_add_u64 v[38:39], v[2:3], 0, s[26:27]
	s_mov_b64 s[26:27], 0x3000
	v_lshl_add_u64 v[40:41], v[2:3], 0, s[26:27]
	s_mov_b64 s[26:27], 0x3400
	s_add_u32 s18, s16, 0x48138000
	v_lshl_add_u64 v[42:43], v[2:3], 0, s[26:27]
	s_mov_b64 s[26:27], 0x3800
	s_addc_u32 s19, s17, 0
	v_lshl_add_u64 v[44:45], v[2:3], 0, s[26:27]
	s_mov_b64 s[26:27], 0x3c00
	s_ashr_i32 s23, s22, 31
	v_lshl_add_u64 v[46:47], v[2:3], 0, s[26:27]
	s_lshl_b32 s26, s22, 1
	s_lshl_b64 s[28:29], s[22:23], 12
	v_readlane_b32 s27, v253, 30
	s_add_u32 s27, s27, s14
	v_readlane_b32 s30, v253, 31
	s_addc_u32 s30, s30, s15
	s_add_u32 s28, s27, s28
	s_addc_u32 s29, s30, s29
	v_lshl_add_u64 v[48:49], v[34:35], 3, s[28:29]
	s_lshl_b64 s[28:29], s[22:23], 11
	v_readlane_b32 s23, v253, 34
	s_add_u32 s23, s23, s14
	v_readlane_b32 s27, v253, 35
	s_addc_u32 s27, s27, s15
	s_add_u32 s28, s23, s28
	v_lshl_add_u32 v37, v34, 6, 0
	s_addc_u32 s29, s27, s29
	v_add_u32_e32 v52, 0x1000, v37
	v_lshl_add_u64 v[50:51], v[34:35], 2, s[28:29]
	v_readlane_b32 s23, v253, 20
	s_mov_b32 s30, s22
	global_load_dwordx4 v[108:111], v[38:39], off
	global_load_dwordx4 v[112:115], v[38:39], off offset:1024
	global_load_dwordx4 v[116:119], v[38:39], off offset:2048
	global_load_dwordx4 v[120:123], v[38:39], off offset:3072
	global_load_dwordx4 v[124:127], v[40:41], off
	global_load_dwordx4 v[128:131], v[42:43], off
	global_load_dwordx4 v[132:135], v[44:45], off
	global_load_dwordx4 v[136:139], v[46:47], off
	global_load_dwordx2 v[140:141], v[48:49], off offset:-2048
	global_load_dwordx2 v[154:155], v[48:49], off offset:1536
	global_load_dwordx2 v[142:143], v[48:49], off offset:-1536
	global_load_dwordx2 v[144:145], v[48:49], off offset:-1024
	global_load_dwordx2 v[146:147], v[48:49], off offset:-512
	global_load_dwordx2 v[148:149], v[48:49], off
	global_load_dwordx2 v[150:151], v[48:49], off offset:512
	global_load_dwordx2 v[152:153], v[48:49], off offset:1024
	s_branch .LBB0_1475

; __device__ __forceinline__ unsigned pk4_fp8(float a, float b, float c, float d) { int w = 0; w = __builtin_amdgcn_cvt_pk_fp8_f32(a, b, w, false); w = __builtin_amdgcn_cvt_pk_fp8_f32(c, d, w, true); return (unsigned)w; }
; #define GAS __attribute__((address_space(1)))
; #define LAS __attribute__((address_space(3)))
; __device__ __forceinline__ f32x4 bf4_to_f32(u32x2_g a) { return (f32x4){__uint_as_float(a.x << 16), __uint_as_float(a.x & 0xffff0000u), __uint_as_float(a.y << 16), __uint_as_float(a.y & 0xffff0000u)}; }
; #define lane (lane_id())
; __device__ __forceinline__ void router_phase(const Ptrs& P, const float* gain, LAS unsigned char* lds, int vcu, int G, int tid, int wave, int lane) {
;     ...
;     for (int m = gw; m < M; m += NGW, li += NWAVES) {
;         const GAS u32x2_g* xr = (const GAS u32x2_g*)(P.H + (size_t)m * D) + lane;
;         f32x4 v[8]; float s = 0.f;
; #pragma unroll
;         for (int j = 0; j < 8; ++j) { v[j] = bf4_to_f32(xr[64 * j]); s += (v[j].x * v[j].x + v[j].y * v[j].y) + (v[j].z * v[j].z + v[j].w * v[j].w); }
;         const float r = 1.0f / sqrtf(wave_sum(s) * (1.0f / D) + EPS);
;         float lg[8];
; #pragma unroll
;         for (int e = 0; e < 8; ++e) lg[e] = 0.f;
;         GAS unsigned* o4 = (GAS unsigned*)(P.AB8 + (size_t)m * D) + lane;
; #pragma unroll
;         for (int j = 0; j < 8; ++j) { const f32x4 g = ((const GAS f32x4*)gain)[lane + 64 * j];
;             const float f0 = v[j].x * r * g.x, f1 = v[j].y * r * g.y, f2 = v[j].z * r * g.z, f3 = v[j].w * r * g.w;
;             o4[64 * j] = pg8::pk4_fp8(f0, f1, f2, f3);
;             const LAS f32x4* rw = LT + 256 * j + 4 * lane;
;             const f32x4 a0 = rw[0], a1 = rw[D], b0 = rw[1], b1 = rw[D + 1], c0 = rw[2], c1 = rw[D + 2], d0 = rw[3], d1 = rw[D + 3];
.LBB0_1475:
	s_waitcnt vmcnt(7)
	v_and_b32_e32 v33, 0xffff0000, v140
	v_and_b32_e32 v31, 0xffff0000, v141
	v_lshlrev_b32_e32 v35, 16, v140
	v_lshlrev_b32_e32 v32, 16, v141
	v_mul_f32_e32 v2, v33, v33
	v_mul_f32_e32 v3, v31, v31
	v_fmac_f32_e32 v2, v35, v35
	v_fmac_f32_e32 v3, v32, v32
	v_add_f32_e32 v4, v2, v3
	s_waitcnt vmcnt(6)
	v_lshlrev_b32_e32 v5, 16, v154
	s_waitcnt vmcnt(5)
	v_and_b32_e32 v29, 0xffff0000, v142
	v_and_b32_e32 v27, 0xffff0000, v143
	v_lshlrev_b32_e32 v30, 16, v142
	v_lshlrev_b32_e32 v28, 16, v143
	v_mul_f32_e32 v2, v29, v29
	v_mul_f32_e32 v3, v27, v27
	v_fmac_f32_e32 v2, v30, v30
	v_fmac_f32_e32 v3, v28, v28
	v_add_f32_e32 v2, v2, v3
	v_add_f32_e32 v4, v4, v2
	s_waitcnt vmcnt(4)
	v_and_b32_e32 v25, 0xffff0000, v144
	v_and_b32_e32 v23, 0xffff0000, v145
	v_lshlrev_b32_e32 v26, 16, v144
	v_lshlrev_b32_e32 v24, 16, v145
	v_mul_f32_e32 v2, v25, v25
	v_mul_f32_e32 v3, v23, v23
	v_fmac_f32_e32 v2, v26, v26
	v_fmac_f32_e32 v3, v24, v24
	v_add_f32_e32 v2, v2, v3
	v_add_f32_e32 v4, v4, v2
	s_waitcnt vmcnt(3)
	v_and_b32_e32 v21, 0xffff0000, v146
	v_and_b32_e32 v19, 0xffff0000, v147
	v_lshlrev_b32_e32 v22, 16, v146
	v_lshlrev_b32_e32 v20, 16, v147
	v_mul_f32_e32 v2, v21, v21
	v_mul_f32_e32 v3, v19, v19
	v_fmac_f32_e32 v2, v22, v22
	v_fmac_f32_e32 v3, v20, v20
	v_add_f32_e32 v2, v2, v3
	v_add_f32_e32 v4, v4, v2
	s_waitcnt vmcnt(2)
	v_and_b32_e32 v17, 0xffff0000, v148
	v_and_b32_e32 v15, 0xffff0000, v149
	v_lshlrev_b32_e32 v18, 16, v148
	v_lshlrev_b32_e32 v16, 16, v149
	v_mul_f32_e32 v2, v17, v17
	v_mul_f32_e32 v3, v15, v15
	v_fmac_f32_e32 v2, v18, v18
	v_fmac_f32_e32 v3, v16, v16
	v_add_f32_e32 v2, v2, v3
	v_add_f32_e32 v4, v4, v2
	s_waitcnt vmcnt(1)
	v_and_b32_e32 v13, 0xffff0000, v150
	v_and_b32_e32 v11, 0xffff0000, v151
	v_lshlrev_b32_e32 v14, 16, v150
	v_lshlrev_b32_e32 v12, 16, v151
	v_mul_f32_e32 v2, v13, v13
	v_mul_f32_e32 v3, v11, v11
	v_fmac_f32_e32 v2, v14, v14
	v_fmac_f32_e32 v3, v12, v12
	v_add_f32_e32 v2, v2, v3
	v_add_f32_e32 v4, v4, v2
	s_waitcnt vmcnt(0)
	v_and_b32_e32 v9, 0xffff0000, v152
	v_and_b32_e32 v7, 0xffff0000, v153
	v_lshlrev_b32_e32 v10, 16, v152
	v_lshlrev_b32_e32 v8, 16, v153
	v_mul_f32_e32 v2, v9, v9
	v_mul_f32_e32 v3, v7, v7
	v_fmac_f32_e32 v2, v10, v10
	v_fmac_f32_e32 v3, v8, v8
	v_add_f32_e32 v2, v2, v3
	v_add_f32_e32 v6, v4, v2
	v_and_b32_e32 v4, 0xffff0000, v154
	v_and_b32_e32 v2, 0xffff0000, v155
	v_lshlrev_b32_e32 v3, 16, v155
	v_readlane_b32 s98, v253, 32
	v_readlane_b32 s99, v253, 33
	s_nop 1
	v_lshl_add_u64 v[156:157], v[48:49], 0, s[98:99]
	global_load_dwordx2 v[140:141], v[156:157], off offset:-2048
	global_load_dwordx2 v[154:155], v[156:157], off offset:1536
	global_load_dwordx2 v[142:143], v[156:157], off offset:-1536
	global_load_dwordx2 v[144:145], v[156:157], off offset:-1024
	global_load_dwordx2 v[146:147], v[156:157], off offset:-512
	global_load_dwordx2 v[148:149], v[156:157], off
	global_load_dwordx2 v[150:151], v[156:157], off offset:512
	global_load_dwordx2 v[152:153], v[156:157], off offset:1024
	v_mul_f32_e32 v53, v4, v4
	v_mul_f32_e32 v54, v2, v2
	v_fmac_f32_e32 v53, v5, v5
	v_fmac_f32_e32 v54, v3, v3
	v_add_f32_e32 v53, v53, v54
	v_add_f32_e32 v6, v6, v53
	s_nop 1
	v_add_f32_dpp v6, v6, v6 quad_perm:[1,0,3,2] row_mask:0xf bank_mask:0xf bound_ctrl:1
	s_nop 1
	v_add_f32_dpp v6, v6, v6 quad_perm:[2,3,0,1] row_mask:0xf bank_mask:0xf bound_ctrl:1
	ds_swizzle_b32 v53, v6 offset:swizzle(SWAP,4)
	s_waitcnt lgkmcnt(0)
	v_add_f32_e32 v6, v6, v53
	ds_swizzle_b32 v53, v6 offset:swizzle(SWAP,8)
	s_waitcnt lgkmcnt(0)
	v_add_f32_e32 v6, v6, v53
	ds_swizzle_b32 v53, v6 offset:swizzle(SWAP,16)
	s_waitcnt lgkmcnt(0)
	v_add_f32_e32 v6, v6, v53
	v_mov_b32_e32 v53, v6
	s_nop 1
	v_permlane32_swap_b32_e32 v6, v53
	v_add_f32_e32 v6, v6, v53
	v_fmamk_f32 v6, v6, 0x3a000000, v204
	v_cmp_gt_f32_e32 vcc, s9, v6
	v_mul_f32_e32 v53, 0x4f800000, v6
	s_nop 0
	v_cndmask_b32_e32 v6, v6, v53, vcc
	v_sqrt_f32_e32 v53, v6
	s_nop 0
	v_add_u32_e32 v54, -1, v53
	v_fma_f32 v55, -v54, v53, v6
	v_cmp_ge_f32_e64 s[40:41], 0, v55
	v_add_u32_e32 v55, 1, v53
	s_nop 0
	v_cndmask_b32_e64 v54, v53, v54, s[40:41]
	v_fma_f32 v53, -v55, v53, v6
	v_cmp_lt_f32_e64 s[40:41], 0, v53
	s_nop 1
	v_cndmask_b32_e64 v53, v54, v55, s[40:41]
	v_mul_f32_e32 v54, 0x37800000, v53
	v_cndmask_b32_e32 v53, v53, v54, vcc
	v_cmp_class_f32_e32 vcc, v6, v205
	s_nop 1
	v_cndmask_b32_e32 v6, v53, v6, vcc
	v_div_scale_f32 v53, s[28:29], v6, v6, 1.0
	v_rcp_f32_e32 v54, v53
	s_nop 0
	v_fma_f32 v55, -v53, v54, 1.0
	v_fmac_f32_e32 v54, v55, v54
	v_div_scale_f32 v55, vcc, 1.0, v6, 1.0
	v_mul_f32_e32 v56, v55, v54
	v_fma_f32 v57, -v53, v56, v55
	v_fmac_f32_e32 v56, v57, v54
	v_fma_f32 v53, -v53, v56, v55
	v_div_fmas_f32 v53, v53, v54, v56
	v_div_fixup_f32 v6, v53, v6, 1.0
	v_mul_f32_e32 v35, v6, v35
	v_mul_f32_e32 v33, v6, v33
	v_mov_b32_e32 v53, v1
	v_mul_f32_e32 v32, v6, v32
	v_mul_f32_e32 v31, v6, v31
	v_mul_f32_e32 v30, v6, v30
	v_mul_f32_e32 v29, v6, v29
	v_mul_f32_e32 v28, v6, v28
	v_mul_f32_e32 v27, v6, v27
	v_mul_f32_e32 v26, v6, v26
	v_mul_f32_e32 v25, v6, v25
	v_mul_f32_e32 v24, v6, v24
	v_mul_f32_e32 v23, v6, v23
	v_mul_f32_e32 v22, v6, v22
	v_mul_f32_e32 v21, v6, v21
	v_mul_f32_e32 v20, v6, v20
	v_mul_f32_e32 v19, v6, v19
	v_mul_f32_e32 v18, v6, v18
	v_mul_f32_e32 v17, v6, v17
	v_mul_f32_e32 v16, v6, v16
	v_mul_f32_e32 v15, v6, v15
	v_mul_f32_e32 v14, v6, v14
	v_mul_f32_e32 v13, v6, v13
	v_mul_f32_e32 v12, v6, v12
	v_mul_f32_e32 v11, v6, v11
	v_mul_f32_e32 v10, v6, v10
	v_mul_f32_e32 v9, v6, v9
	v_mul_f32_e32 v8, v6, v8
	v_mul_f32_e32 v7, v6, v7
	v_mul_f32_e32 v5, v6, v5
	v_mul_f32_e32 v4, v6, v4
	v_mul_f32_e32 v2, v6, v2
	v_mul_f32_e32 v3, v6, v3
	v_mul_f32_e32 v35, v108, v35
	v_mul_f32_e32 v33, v109, v33
	v_cvt_pk_fp8_f32 v53, v35, v33
	v_mul_f32_e32 v32, v110, v32
	v_mul_f32_e32 v31, v111, v31
	v_cvt_pk_fp8_f32 v53, v32, v31 op_sel:[0,0,1]
	global_store_dword v[50:51], v53, off offset:-1024 sc0 sc1
	ds_read_b128 v[54:57], v37 offset:36864
	ds_read_b128 v[58:61], v37 offset:36880
	ds_read_b128 v[62:65], v37 offset:36896
	ds_read_b128 v[66:69], v37 offset:4096
	ds_read_b128 v[70:73], v37 offset:4112
	ds_read_b128 v[74:77], v37 offset:4128
	ds_read_b128 v[78:81], v37 offset:4144
	ds_read_b128 v[82:85], v37 offset:36912
	s_waitcnt lgkmcnt(6)
; __device__ __forceinline__ unsigned pk4_fp8(float a, float b, float c, float d) { int w = 0; w = __builtin_amdgcn_cvt_pk_fp8_f32(a, b, w, false); w = __builtin_amdgcn_cvt_pk_fp8_f32(c, d, w, true); return (unsigned)w; }
; #define GAS __attribute__((address_space(1)))
; #define LAS __attribute__((address_space(3)))
; #define lane (lane_id())
; __device__ __forceinline__ void router_phase(const Ptrs& P, const float* gain, LAS unsigned char* lds, int vcu, int G, int tid, int wave, int lane) {
;     ...
;         for (int j = 0; j < 8; ++j) { const f32x4 g = ((const GAS f32x4*)gain)[lane + 64 * j];
;             const float f0 = v[j].x * r * g.x, f1 = v[j].y * r * g.y, f2 = v[j].z * r * g.z, f3 = v[j].w * r * g.w;
;             o4[64 * j] = pg8::pk4_fp8(f0, f1, f2, f3);
;             const LAS f32x4* rw = LT + 256 * j + 4 * lane;
;             const f32x4 a0 = rw[0], a1 = rw[D], b0 = rw[1], b1 = rw[D + 1], c0 = rw[2], c1 = rw[D + 2], d0 = rw[3], d1 = rw[D + 3];
;             lg[0] += f0 * a0.x + f1 * b0.x + f2 * c0.x + f3 * d0.x; lg[1] += f0 * a0.y + f1 * b0.y + f2 * c0.y + f3 * d0.y;
;             lg[2] += f0 * a0.z + f1 * b0.z + f2 * c0.z + f3 * d0.z; lg[3] += f0 * a0.w + f1 * b0.w + f2 * c0.w + f3 * d0.w;
;             lg[4] += f0 * a1.x + f1 * b1.x + f2 * c1.x + f3 * d1.x; lg[5] += f0 * a1.y + f1 * b1.y + f2 * c1.y + f3 * d1.y;
;             lg[6] += f0 * a1.z + f1 * b1.z + f2 * c1.z + f3 * d1.z; lg[7] += f0 * a1.w + f1 * b1.w + f2 * c1.w + f3 * d1.w; }
	v_mul_f32_e32 v58, v33, v58
	s_waitcnt lgkmcnt(3)
	v_mul_f32_e32 v53, v70, v33
	v_fmac_f32_e32 v53, v66, v35
	v_mul_f32_e32 v66, v71, v33
	v_fmac_f32_e32 v66, v67, v35
	v_fmac_f32_e32 v58, v54, v35
	v_mul_f32_e32 v54, v33, v59
	s_waitcnt lgkmcnt(2)
	v_fmac_f32_e32 v66, v32, v75
	v_fmac_f32_e32 v54, v55, v35
	s_waitcnt lgkmcnt(1)
	v_fmac_f32_e32 v66, v31, v79
	v_fmac_f32_e32 v54, v32, v63
	v_add_f32_e32 v86, 0, v66
	v_mul_f32_e32 v66, v72, v33
	s_waitcnt lgkmcnt(0)
	v_fmac_f32_e32 v54, v31, v83
	v_fmac_f32_e32 v66, v68, v35
	v_add_f32_e32 v83, 0, v54
	v_mul_f32_e32 v54, v33, v60
	v_fmac_f32_e32 v66, v32, v76
	v_fmac_f32_e32 v54, v56, v35
	v_fmac_f32_e32 v66, v31, v80
	v_fmac_f32_e32 v54, v32, v64
	v_add_f32_e32 v87, 0, v66
	v_mul_f32_e32 v66, v73, v33
	v_fmac_f32_e32 v54, v31, v84
	v_mul_f32_e32 v33, v33, v61
	v_add_f32_e32 v84, 0, v54
	v_fmac_f32_e32 v33, v57, v35
	v_fmac_f32_e32 v33, v32, v65
	v_fmac_f32_e32 v66, v69, v35
	v_fmac_f32_e32 v33, v31, v85
	v_fmac_f32_e32 v53, v32, v74
	v_fmac_f32_e32 v66, v32, v77
	v_fmac_f32_e32 v58, v32, v62
	v_add_f32_e32 v32, 0, v33
	v_fmac_f32_e32 v66, v31, v81
	v_fmac_f32_e32 v58, v31, v82
	v_fmac_f32_e32 v53, v31, v78
	v_add_f32_e32 v88, 0, v66
	v_add_f32_e32 v82, 0, v58
	v_add_f32_e32 v53, 0, v53
	v_mul_f32_e32 v33, v30, v112
	v_mul_f32_e32 v35, v29, v113
	v_mul_f32_e32 v85, v28, v114
	v_mov_b32_e32 v28, v1
	v_cvt_pk_fp8_f32 v28, v33, v35
	v_mul_f32_e32 v27, v27, v115
	v_cvt_pk_fp8_f32 v28, v85, v27 op_sel:[0,0,1]
	global_store_dword v[50:51], v28, off offset:-768 sc0 sc1
	ds_read_b128 v[28:31], v37 offset:40960
	ds_read_b128 v[54:57], v37 offset:40976
	ds_read_b128 v[58:61], v37 offset:40992
	ds_read_b128 v[62:65], v37 offset:8192
	ds_read_b128 v[66:69], v37 offset:8208
	ds_read_b128 v[70:73], v37 offset:8224
	ds_read_b128 v[74:77], v37 offset:8240
	ds_read_b128 v[78:81], v37 offset:41008
	s_waitcnt lgkmcnt(6)
	v_mul_f32_e32 v54, v35, v54
	v_fmac_f32_e32 v54, v33, v28
	v_mul_f32_e32 v28, v35, v55
	v_fmac_f32_e32 v28, v33, v29
	s_waitcnt lgkmcnt(5)
	v_fmac_f32_e32 v28, v85, v59
	s_waitcnt lgkmcnt(0)
	v_fmac_f32_e32 v28, v27, v79
	v_add_f32_e32 v79, v83, v28
	v_mul_f32_e32 v28, v35, v56
	v_fmac_f32_e32 v28, v33, v30
	v_fmac_f32_e32 v28, v85, v60
	v_fmac_f32_e32 v28, v27, v80
	v_add_f32_e32 v80, v84, v28
	v_mul_f32_e32 v28, v35, v57
	v_fmac_f32_e32 v28, v33, v31
	v_fmac_f32_e32 v28, v85, v61
	v_fmac_f32_e32 v28, v27, v81
	v_add_f32_e32 v32, v32, v28
	v_mul_f32_e32 v66, v35, v66
	v_fmac_f32_e32 v66, v33, v62
	v_mul_f32_e32 v62, v35, v67
	v_fmac_f32_e32 v62, v33, v63
	v_fmac_f32_e32 v62, v85, v71
	v_fmac_f32_e32 v62, v27, v75
	v_add_f32_e32 v86, v86, v62
	v_mul_f32_e32 v62, v35, v68
	v_fmac_f32_e32 v62, v33, v64
	v_fmac_f32_e32 v62, v85, v72
	v_fmac_f32_e32 v62, v27, v76
	v_add_f32_e32 v87, v87, v62
	v_mul_f32_e32 v62, v35, v69
	v_fmac_f32_e32 v62, v33, v65
	v_fmac_f32_e32 v66, v85, v70
	v_fmac_f32_e32 v62, v85, v73
	v_fmac_f32_e32 v54, v85, v58
	v_fmac_f32_e32 v66, v27, v74
	v_fmac_f32_e32 v62, v27, v77
	v_fmac_f32_e32 v54, v27, v78
	v_add_f32_e32 v53, v53, v66
	v_add_f32_e32 v88, v88, v62
	v_add_f32_e32 v78, v82, v54
	v_mul_f32_e32 v33, v26, v116
	v_mul_f32_e32 v35, v25, v117
	v_mul_f32_e32 v81, v24, v118
	v_mov_b32_e32 v24, v1
	v_cvt_pk_fp8_f32 v24, v33, v35
	v_mul_f32_e32 v23, v23, v119
	v_cvt_pk_fp8_f32 v24, v81, v23 op_sel:[0,0,1]
	global_store_dword v[50:51], v24, off offset:-512 sc0 sc1
	ds_read_b128 v[24:27], v37 offset:45056
	ds_read_b128 v[28:31], v37 offset:45072
	ds_read_b128 v[54:57], v37 offset:45088
	ds_read_b128 v[58:61], v37 offset:12288
	ds_read_b128 v[62:65], v37 offset:12304
	ds_read_b128 v[66:69], v37 offset:12320
	ds_read_b128 v[70:73], v37 offset:12336
	ds_read_b128 v[74:77], v37 offset:45104
	s_waitcnt lgkmcnt(6)
	v_mul_f32_e32 v28, v35, v28
	v_fmac_f32_e32 v28, v33, v24
	v_mul_f32_e32 v24, v35, v29
	v_fmac_f32_e32 v24, v33, v25
	s_waitcnt lgkmcnt(5)
	v_fmac_f32_e32 v24, v81, v55
	s_waitcnt lgkmcnt(0)
	v_fmac_f32_e32 v24, v23, v75
	v_add_f32_e32 v75, v79, v24
	v_mul_f32_e32 v24, v35, v30
	v_fmac_f32_e32 v24, v33, v26
	v_fmac_f32_e32 v24, v81, v56
	v_fmac_f32_e32 v24, v23, v76
	v_add_f32_e32 v76, v80, v24
	v_mul_f32_e32 v24, v35, v31
	v_fmac_f32_e32 v24, v33, v27
	v_fmac_f32_e32 v24, v81, v57
	v_fmac_f32_e32 v24, v23, v77
	v_add_f32_e32 v32, v32, v24
	v_mul_f32_e32 v62, v35, v62
	v_fmac_f32_e32 v62, v33, v58
	v_mul_f32_e32 v58, v35, v63
	v_fmac_f32_e32 v58, v33, v59
	v_fmac_f32_e32 v58, v81, v67
	v_fmac_f32_e32 v58, v23, v71
	v_add_f32_e32 v82, v86, v58
	v_mul_f32_e32 v58, v35, v64
	v_fmac_f32_e32 v58, v33, v60
	v_fmac_f32_e32 v58, v81, v68
	v_fmac_f32_e32 v58, v23, v72
	v_add_f32_e32 v83, v87, v58
	v_mul_f32_e32 v58, v35, v65
	v_fmac_f32_e32 v58, v33, v61
	v_fmac_f32_e32 v62, v81, v66
	v_fmac_f32_e32 v58, v81, v69
	v_fmac_f32_e32 v28, v81, v54
	v_fmac_f32_e32 v62, v23, v70
	v_fmac_f32_e32 v58, v23, v73
	v_fmac_f32_e32 v28, v23, v74
	v_add_f32_e32 v53, v53, v62
	v_add_f32_e32 v84, v88, v58
	v_add_f32_e32 v74, v78, v28
	v_mul_f32_e32 v33, v22, v120
	v_mul_f32_e32 v35, v21, v121
	v_mul_f32_e32 v77, v20, v122
	v_mov_b32_e32 v20, v1
	v_cvt_pk_fp8_f32 v20, v33, v35
	v_mul_f32_e32 v19, v19, v123
	v_cvt_pk_fp8_f32 v20, v77, v19 op_sel:[0,0,1]
	global_store_dword v[50:51], v20, off offset:-256 sc0 sc1
	ds_read_b128 v[20:23], v37 offset:49152
	ds_read_b128 v[24:27], v37 offset:49168
	ds_read_b128 v[28:31], v37 offset:49184
	ds_read_b128 v[54:57], v37 offset:16384
	ds_read_b128 v[58:61], v37 offset:16400
	ds_read_b128 v[62:65], v37 offset:16416
	ds_read_b128 v[66:69], v37 offset:16432
	ds_read_b128 v[70:73], v37 offset:49200
	s_waitcnt lgkmcnt(6)
; __device__ __forceinline__ unsigned pk4_fp8(float a, float b, float c, float d) { int w = 0; w = __builtin_amdgcn_cvt_pk_fp8_f32(a, b, w, false); w = __builtin_amdgcn_cvt_pk_fp8_f32(c, d, w, true); return (unsigned)w; }
; #define GAS __attribute__((address_space(1)))
; #define LAS __attribute__((address_space(3)))
; #define lane (lane_id())
; __device__ __forceinline__ void router_phase(const Ptrs& P, const float* gain, LAS unsigned char* lds, int vcu, int G, int tid, int wave, int lane) {
;     ...
;         for (int j = 0; j < 8; ++j) { const f32x4 g = ((const GAS f32x4*)gain)[lane + 64 * j];
;             const float f0 = v[j].x * r * g.x, f1 = v[j].y * r * g.y, f2 = v[j].z * r * g.z, f3 = v[j].w * r * g.w;
;             o4[64 * j] = pg8::pk4_fp8(f0, f1, f2, f3);
;             const LAS f32x4* rw = LT + 256 * j + 4 * lane;
;             const f32x4 a0 = rw[0], a1 = rw[D], b0 = rw[1], b1 = rw[D + 1], c0 = rw[2], c1 = rw[D + 2], d0 = rw[3], d1 = rw[D + 3];
;             lg[0] += f0 * a0.x + f1 * b0.x + f2 * c0.x + f3 * d0.x; lg[1] += f0 * a0.y + f1 * b0.y + f2 * c0.y + f3 * d0.y;
;             lg[2] += f0 * a0.z + f1 * b0.z + f2 * c0.z + f3 * d0.z; lg[3] += f0 * a0.w + f1 * b0.w + f2 * c0.w + f3 * d0.w;
;             lg[4] += f0 * a1.x + f1 * b1.x + f2 * c1.x + f3 * d1.x; lg[5] += f0 * a1.y + f1 * b1.y + f2 * c1.y + f3 * d1.y;
;             lg[6] += f0 * a1.z + f1 * b1.z + f2 * c1.z + f3 * d1.z; lg[7] += f0 * a1.w + f1 * b1.w + f2 * c1.w + f3 * d1.w; }
	v_mul_f32_e32 v24, v35, v24
	v_fmac_f32_e32 v24, v33, v20
	v_mul_f32_e32 v20, v35, v25
	v_fmac_f32_e32 v20, v33, v21
	s_waitcnt lgkmcnt(5)
	v_fmac_f32_e32 v20, v77, v29
	s_waitcnt lgkmcnt(0)
	v_fmac_f32_e32 v20, v19, v71
	v_add_f32_e32 v71, v75, v20
	v_mul_f32_e32 v20, v35, v26
	v_fmac_f32_e32 v20, v33, v22
	v_fmac_f32_e32 v20, v77, v30
	v_fmac_f32_e32 v20, v19, v72
	v_add_f32_e32 v72, v76, v20
	v_mul_f32_e32 v20, v35, v27
	v_fmac_f32_e32 v20, v33, v23
	v_fmac_f32_e32 v20, v77, v31
	v_fmac_f32_e32 v20, v19, v73
	v_add_f32_e32 v32, v32, v20
	v_mul_f32_e32 v58, v35, v58
	v_fmac_f32_e32 v58, v33, v54
	v_mul_f32_e32 v54, v35, v59
	v_fmac_f32_e32 v54, v33, v55
	v_fmac_f32_e32 v54, v77, v63
	v_fmac_f32_e32 v54, v19, v67
	v_add_f32_e32 v78, v82, v54
	v_mul_f32_e32 v54, v35, v60
	v_fmac_f32_e32 v54, v33, v56
	v_fmac_f32_e32 v54, v77, v64
	v_fmac_f32_e32 v54, v19, v68
	v_add_f32_e32 v79, v83, v54
	v_mul_f32_e32 v54, v35, v61
	v_fmac_f32_e32 v54, v33, v57
	v_fmac_f32_e32 v58, v77, v62
	v_fmac_f32_e32 v54, v77, v65
	v_fmac_f32_e32 v24, v77, v28
	v_fmac_f32_e32 v58, v19, v66
	v_fmac_f32_e32 v54, v19, v69
	v_fmac_f32_e32 v24, v19, v70
	v_add_f32_e32 v53, v53, v58
	v_add_f32_e32 v80, v84, v54
	v_add_f32_e32 v70, v74, v24
	v_mul_f32_e32 v33, v18, v124
	v_mul_f32_e32 v35, v17, v125
	v_mul_f32_e32 v73, v16, v126
	v_mov_b32_e32 v16, v1
	v_cvt_pk_fp8_f32 v16, v33, v35
	v_mul_f32_e32 v15, v15, v127
	v_cvt_pk_fp8_f32 v16, v73, v15 op_sel:[0,0,1]
	global_store_dword v[50:51], v16, off sc0 sc1
	ds_read_b128 v[16:19], v37 offset:53248
	ds_read_b128 v[20:23], v37 offset:53264
	ds_read_b128 v[24:27], v37 offset:53280
	ds_read_b128 v[28:31], v37 offset:20480
	ds_read_b128 v[54:57], v37 offset:20496
	ds_read_b128 v[58:61], v37 offset:20512
	ds_read_b128 v[62:65], v37 offset:20528
	ds_read_b128 v[66:69], v37 offset:53296
	s_waitcnt lgkmcnt(6)
	v_mul_f32_e32 v20, v35, v20
	v_fmac_f32_e32 v20, v33, v16
	v_mul_f32_e32 v16, v35, v21
	v_fmac_f32_e32 v16, v33, v17
	s_waitcnt lgkmcnt(5)
	v_fmac_f32_e32 v16, v73, v25
	s_waitcnt lgkmcnt(0)
	v_fmac_f32_e32 v16, v15, v67
	v_add_f32_e32 v67, v71, v16
	v_mul_f32_e32 v16, v35, v22
	v_fmac_f32_e32 v16, v33, v18
	v_fmac_f32_e32 v16, v73, v26
	v_fmac_f32_e32 v16, v15, v68
	v_add_f32_e32 v68, v72, v16
	v_mul_f32_e32 v16, v35, v23
	v_fmac_f32_e32 v16, v33, v19
	v_fmac_f32_e32 v16, v73, v27
	v_fmac_f32_e32 v16, v15, v69
	v_add_f32_e32 v32, v32, v16
	v_mul_f32_e32 v54, v35, v54
	v_fmac_f32_e32 v54, v33, v28
	v_mul_f32_e32 v28, v35, v55
	v_fmac_f32_e32 v28, v33, v29
	v_fmac_f32_e32 v28, v73, v59
	v_fmac_f32_e32 v28, v15, v63
	v_add_f32_e32 v74, v78, v28
	v_mul_f32_e32 v28, v35, v56
	v_fmac_f32_e32 v28, v33, v30
	v_fmac_f32_e32 v28, v73, v60
	v_fmac_f32_e32 v28, v15, v64
	v_add_f32_e32 v75, v79, v28
	v_mul_f32_e32 v28, v35, v57
	v_fmac_f32_e32 v28, v33, v31
	v_fmac_f32_e32 v54, v73, v58
	v_fmac_f32_e32 v28, v73, v61
	v_fmac_f32_e32 v20, v73, v24
	v_fmac_f32_e32 v54, v15, v62
	v_fmac_f32_e32 v28, v15, v65
	v_fmac_f32_e32 v20, v15, v66
	v_add_f32_e32 v53, v53, v54
	v_add_f32_e32 v76, v80, v28
	v_add_f32_e32 v66, v70, v20
	v_mul_f32_e32 v33, v14, v128
	v_mul_f32_e32 v35, v13, v129
	v_mul_f32_e32 v69, v12, v130
	v_mov_b32_e32 v12, v1
	v_cvt_pk_fp8_f32 v12, v33, v35
	v_mul_f32_e32 v11, v11, v131
	v_cvt_pk_fp8_f32 v12, v69, v11 op_sel:[0,0,1]
	global_store_dword v[50:51], v12, off offset:256 sc0 sc1
	ds_read_b128 v[12:15], v37 offset:57344
	ds_read_b128 v[16:19], v37 offset:57360
	ds_read_b128 v[20:23], v37 offset:57376
	ds_read_b128 v[24:27], v37 offset:24576
	ds_read_b128 v[28:31], v37 offset:24592
	ds_read_b128 v[54:57], v37 offset:24608
	ds_read_b128 v[58:61], v37 offset:24624
	ds_read_b128 v[62:65], v37 offset:57392
	s_waitcnt lgkmcnt(6)
	v_mul_f32_e32 v16, v35, v16
	v_fmac_f32_e32 v16, v33, v12
	v_mul_f32_e32 v12, v35, v17
	v_fmac_f32_e32 v12, v33, v13
	s_waitcnt lgkmcnt(5)
	v_fmac_f32_e32 v12, v69, v21
	s_waitcnt lgkmcnt(0)
	v_fmac_f32_e32 v12, v11, v63
	v_add_f32_e32 v71, v67, v12
	v_mul_f32_e32 v12, v35, v18
	v_fmac_f32_e32 v12, v33, v14
	v_fmac_f32_e32 v12, v69, v22
	v_fmac_f32_e32 v12, v11, v64
	v_add_f32_e32 v68, v68, v12
	v_mul_f32_e32 v12, v35, v19
	v_fmac_f32_e32 v12, v33, v15
	v_fmac_f32_e32 v12, v69, v23
	v_fmac_f32_e32 v12, v11, v65
	v_add_f32_e32 v32, v32, v12
	v_mul_f32_e32 v28, v35, v28
	v_fmac_f32_e32 v28, v33, v24
	v_mul_f32_e32 v24, v35, v29
	v_fmac_f32_e32 v24, v33, v25
	v_fmac_f32_e32 v24, v69, v55
	v_fmac_f32_e32 v28, v69, v54
	v_fmac_f32_e32 v24, v11, v59
	v_fmac_f32_e32 v28, v11, v58
	v_add_f32_e32 v58, v74, v24
	v_mul_f32_e32 v24, v35, v30
	v_fmac_f32_e32 v24, v33, v26
	v_fmac_f32_e32 v24, v69, v56
	v_fmac_f32_e32 v24, v11, v60
	v_add_f32_e32 v59, v75, v24
	v_mul_f32_e32 v24, v35, v31
	v_fmac_f32_e32 v24, v33, v27
	v_fmac_f32_e32 v24, v69, v57
	v_fmac_f32_e32 v16, v69, v20
	v_fmac_f32_e32 v24, v11, v61
	v_fmac_f32_e32 v16, v11, v62
	v_add_f32_e32 v53, v53, v28
	v_add_f32_e32 v60, v76, v24
	v_add_f32_e32 v70, v66, v16
	v_mul_f32_e32 v33, v10, v132
	v_mul_f32_e32 v35, v9, v133
	v_mul_f32_e32 v69, v8, v134
	v_mov_b32_e32 v8, v1
	v_cvt_pk_fp8_f32 v8, v33, v35
	v_mul_f32_e32 v7, v7, v135
	v_cvt_pk_fp8_f32 v8, v69, v7 op_sel:[0,0,1]
	global_store_dword v[50:51], v8, off offset:512 sc0 sc1
	ds_read_b128 v[8:11], v37 offset:61440
	ds_read_b128 v[12:15], v37 offset:61456
	ds_read_b128 v[16:19], v37 offset:61472
	ds_read_b128 v[20:23], v37 offset:28672
	ds_read_b128 v[24:27], v37 offset:28688
	ds_read_b128 v[28:31], v37 offset:28704
	ds_read_b128 v[54:57], v37 offset:28720
	ds_read_b128 v[64:67], v37 offset:61488
	s_waitcnt lgkmcnt(6)
	v_mul_f32_e32 v12, v35, v12
	s_waitcnt lgkmcnt(3)
; __device__ __forceinline__ unsigned pk4_fp8(float a, float b, float c, float d) { int w = 0; w = __builtin_amdgcn_cvt_pk_fp8_f32(a, b, w, false); w = __builtin_amdgcn_cvt_pk_fp8_f32(c, d, w, true); return (unsigned)w; }
; #define GAS __attribute__((address_space(1)))
; #define LAS __attribute__((address_space(3)))
; #define lane (lane_id())
; __device__ __forceinline__ void router_phase(const Ptrs& P, const float* gain, LAS unsigned char* lds, int vcu, int G, int tid, int wave, int lane) {
;     ...
;         for (int j = 0; j < 8; ++j) { const f32x4 g = ((const GAS f32x4*)gain)[lane + 64 * j];
;             const float f0 = v[j].x * r * g.x, f1 = v[j].y * r * g.y, f2 = v[j].z * r * g.z, f3 = v[j].w * r * g.w;
;             o4[64 * j] = pg8::pk4_fp8(f0, f1, f2, f3);
;             const LAS f32x4* rw = LT + 256 * j + 4 * lane;
;             const f32x4 a0 = rw[0], a1 = rw[D], b0 = rw[1], b1 = rw[D + 1], c0 = rw[2], c1 = rw[D + 2], d0 = rw[3], d1 = rw[D + 3];
;             lg[0] += f0 * a0.x + f1 * b0.x + f2 * c0.x + f3 * d0.x; lg[1] += f0 * a0.y + f1 * b0.y + f2 * c0.y + f3 * d0.y;
;             lg[2] += f0 * a0.z + f1 * b0.z + f2 * c0.z + f3 * d0.z; lg[3] += f0 * a0.w + f1 * b0.w + f2 * c0.w + f3 * d0.w;
;             lg[4] += f0 * a1.x + f1 * b1.x + f2 * c1.x + f3 * d1.x; lg[5] += f0 * a1.y + f1 * b1.y + f2 * c1.y + f3 * d1.y;
;             lg[6] += f0 * a1.z + f1 * b1.z + f2 * c1.z + f3 * d1.z; lg[7] += f0 * a1.w + f1 * b1.w + f2 * c1.w + f3 * d1.w; }
; #pragma unroll
;         for (int e = 0; e < 8; ++e) lg[e] = wave_sum(lg[e]);
	v_mul_f32_e32 v24, v35, v24
	v_fmac_f32_e32 v24, v33, v20
	v_mul_f32_e32 v20, v35, v25
	v_fmac_f32_e32 v20, v33, v21
	s_waitcnt lgkmcnt(2)
	v_fmac_f32_e32 v20, v69, v29
	s_waitcnt lgkmcnt(1)
	v_fmac_f32_e32 v20, v7, v55
	v_fmac_f32_e32 v12, v33, v8
	v_mul_f32_e32 v8, v35, v13
	v_add_f32_e32 v62, v58, v20
	v_mul_f32_e32 v20, v35, v26
	v_fmac_f32_e32 v8, v33, v9
	v_fmac_f32_e32 v20, v33, v22
	v_fmac_f32_e32 v8, v69, v17
	v_fmac_f32_e32 v20, v69, v30
	s_waitcnt lgkmcnt(0)
	v_fmac_f32_e32 v8, v7, v65
	v_fmac_f32_e32 v20, v7, v56
	v_add_f32_e32 v58, v71, v8
	v_mul_f32_e32 v8, v35, v14
	v_add_f32_e32 v61, v59, v20
	v_mul_f32_e32 v20, v35, v27
	v_fmac_f32_e32 v8, v33, v10
	v_fmac_f32_e32 v20, v33, v23
	v_fmac_f32_e32 v8, v69, v18
	v_fmac_f32_e32 v20, v69, v31
	v_fmac_f32_e32 v8, v7, v66
	v_fmac_f32_e32 v20, v7, v57
	v_add_f32_e32 v57, v68, v8
	v_mul_f32_e32 v8, v35, v15
	v_fmac_f32_e32 v8, v33, v11
	v_fmac_f32_e32 v8, v69, v19
	v_fmac_f32_e32 v8, v7, v67
	v_add_f32_e32 v35, v32, v8
	v_fmac_f32_e32 v24, v69, v28
	v_fmac_f32_e32 v24, v7, v54
	v_add_f32_e32 v63, v53, v24
	v_fmac_f32_e32 v12, v69, v16
	v_fmac_f32_e32 v12, v7, v64
	v_add_f32_e32 v60, v60, v20
	v_add_f32_e32 v59, v70, v12
	v_mul_f32_e32 v55, v5, v136
	v_mul_f32_e32 v56, v4, v137
	v_mul_f32_e32 v53, v2, v139
	v_mov_b32_e32 v2, v1
	v_cvt_pk_fp8_f32 v2, v55, v56
	v_mul_f32_e32 v54, v3, v138
	v_cvt_pk_fp8_f32 v2, v54, v53 op_sel:[0,0,1]
	global_store_dword v[50:51], v2, off offset:768 sc0 sc1
	ds_read_b128 v[6:9], v37 offset:32768
	ds_read_b128 v[14:17], v37 offset:32784
	ds_read_b128 v[26:29], v37 offset:32800
	ds_read_b128 v[30:33], v37 offset:32816
	ds_read_b128 v[2:5], v52 offset:61440
	ds_read_b128 v[22:25], v52 offset:61456
	ds_read_b128 v[18:21], v52 offset:61472
	ds_read_b128 v[10:13], v52 offset:61488
	s_waitcnt lgkmcnt(6)
	v_mul_f32_e32 v14, v56, v14
	v_fmac_f32_e32 v14, v55, v6
	s_waitcnt lgkmcnt(5)
	v_fmac_f32_e32 v14, v54, v26
	s_waitcnt lgkmcnt(4)
	v_fmac_f32_e32 v14, v53, v30
	v_add_f32_e32 v6, v63, v14
	v_mul_f32_e32 v14, v56, v15
	v_fmac_f32_e32 v14, v55, v7
	v_fmac_f32_e32 v14, v54, v27
	v_fmac_f32_e32 v14, v53, v31
	v_add_f32_e32 v7, v62, v14
	v_mul_f32_e32 v14, v56, v16
	v_fmac_f32_e32 v14, v55, v8
	v_fmac_f32_e32 v14, v54, v28
	v_fmac_f32_e32 v14, v53, v32
	v_add_f32_e32 v8, v61, v14
	v_mul_f32_e32 v14, v56, v17
	v_fmac_f32_e32 v14, v55, v9
	v_fmac_f32_e32 v14, v54, v29
	v_fmac_f32_e32 v14, v53, v33
	v_add_f32_e32 v9, v60, v14
	s_waitcnt lgkmcnt(2)
	v_mul_f32_e32 v14, v56, v22
	v_fmac_f32_e32 v14, v55, v2
	v_mul_f32_e32 v2, v56, v23
	v_fmac_f32_e32 v2, v55, v3
	s_waitcnt lgkmcnt(1)
	v_fmac_f32_e32 v14, v54, v18
	v_fmac_f32_e32 v2, v54, v19
	s_waitcnt lgkmcnt(0)
	v_fmac_f32_e32 v14, v53, v10
	v_fmac_f32_e32 v2, v53, v11
	v_add_f32_e32 v10, v59, v14
	v_add_f32_e32 v14, v58, v2
	v_mul_f32_e32 v2, v56, v24
	v_fmac_f32_e32 v2, v55, v4
	v_fmac_f32_e32 v2, v54, v20
	v_fmac_f32_e32 v2, v53, v12
	v_add_f32_e32 v15, v57, v2
	v_mul_f32_e32 v2, v56, v25
	v_fmac_f32_e32 v2, v55, v5
	v_fmac_f32_e32 v2, v54, v21
	v_fmac_f32_e32 v2, v53, v13
	v_add_f32_e32 v16, v35, v2
	v_add_f32_dpp v10, v10, v10 quad_perm:[1,0,3,2] row_mask:0xf bank_mask:0xf bound_ctrl:1
	v_add_f32_dpp v2, v6, v6 quad_perm:[1,0,3,2] row_mask:0xf bank_mask:0xf bound_ctrl:1
	v_add_f32_dpp v6, v8, v8 quad_perm:[1,0,3,2] row_mask:0xf bank_mask:0xf bound_ctrl:1
	v_add_f32_dpp v8, v9, v9 quad_perm:[1,0,3,2] row_mask:0xf bank_mask:0xf bound_ctrl:1
	v_add_f32_dpp v2, v2, v2 quad_perm:[2,3,0,1] row_mask:0xf bank_mask:0xf bound_ctrl:1
	ds_swizzle_b32 v3, v2 offset:swizzle(SWAP,4)
	v_add_f32_dpp v12, v14, v14 quad_perm:[1,0,3,2] row_mask:0xf bank_mask:0xf bound_ctrl:1
	v_add_f32_dpp v14, v15, v15 quad_perm:[1,0,3,2] row_mask:0xf bank_mask:0xf bound_ctrl:1
	v_add_f32_dpp v16, v16, v16 quad_perm:[1,0,3,2] row_mask:0xf bank_mask:0xf bound_ctrl:1
	v_add_f32_dpp v6, v6, v6 quad_perm:[2,3,0,1] row_mask:0xf bank_mask:0xf bound_ctrl:1
	s_waitcnt lgkmcnt(0)
	v_add_f32_e32 v2, v2, v3
	ds_swizzle_b32 v3, v2 offset:swizzle(SWAP,8)
	v_add_f32_dpp v8, v8, v8 quad_perm:[2,3,0,1] row_mask:0xf bank_mask:0xf bound_ctrl:1
	v_add_f32_dpp v10, v10, v10 quad_perm:[2,3,0,1] row_mask:0xf bank_mask:0xf bound_ctrl:1
	v_add_f32_dpp v12, v12, v12 quad_perm:[2,3,0,1] row_mask:0xf bank_mask:0xf bound_ctrl:1
	v_add_f32_dpp v14, v14, v14 quad_perm:[2,3,0,1] row_mask:0xf bank_mask:0xf bound_ctrl:1
	s_waitcnt lgkmcnt(0)
	v_add_f32_e32 v2, v2, v3
	ds_swizzle_b32 v3, v2 offset:swizzle(SWAP,16)
	v_add_f32_dpp v16, v16, v16 quad_perm:[2,3,0,1] row_mask:0xf bank_mask:0xf bound_ctrl:1
	ds_swizzle_b32 v9, v8 offset:swizzle(SWAP,4)
	ds_swizzle_b32 v11, v10 offset:swizzle(SWAP,4)
	ds_swizzle_b32 v13, v12 offset:swizzle(SWAP,4)
	s_waitcnt lgkmcnt(3)
	v_add_f32_e32 v3, v2, v3
	v_add_f32_dpp v2, v7, v7 quad_perm:[1,0,3,2] row_mask:0xf bank_mask:0xf bound_ctrl:1
	ds_swizzle_b32 v7, v6 offset:swizzle(SWAP,4)
	ds_swizzle_b32 v15, v14 offset:swizzle(SWAP,4)
	v_add_f32_dpp v2, v2, v2 quad_perm:[2,3,0,1] row_mask:0xf bank_mask:0xf bound_ctrl:1
	ds_swizzle_b32 v4, v2 offset:swizzle(SWAP,4)
	ds_swizzle_b32 v17, v16 offset:swizzle(SWAP,4)
	s_waitcnt lgkmcnt(3)
	v_add_f32_e32 v6, v6, v7
	v_add_f32_e32 v8, v8, v9
	v_add_f32_e32 v10, v10, v11
	s_waitcnt lgkmcnt(1)
	v_add_f32_e32 v2, v2, v4
	v_add_f32_e32 v12, v12, v13
	v_add_f32_e32 v14, v14, v15
	s_waitcnt lgkmcnt(0)
	v_add_f32_e32 v16, v16, v17
	ds_swizzle_b32 v4, v2 offset:swizzle(SWAP,8)
	ds_swizzle_b32 v7, v6 offset:swizzle(SWAP,8)
	ds_swizzle_b32 v9, v8 offset:swizzle(SWAP,8)
	ds_swizzle_b32 v11, v10 offset:swizzle(SWAP,8)
	ds_swizzle_b32 v13, v12 offset:swizzle(SWAP,8)
	ds_swizzle_b32 v15, v14 offset:swizzle(SWAP,8)
	ds_swizzle_b32 v17, v16 offset:swizzle(SWAP,8)
	s_waitcnt lgkmcnt(6)
; #define LDS_WAIT() asm volatile("s_waitcnt lgkmcnt(0)" ::: "memory")
; #define tid (tid_of(wave))
; #define lane (lane_id())
; __device__ __forceinline__ void router_phase(const Ptrs& P, const float* gain, LAS unsigned char* lds, int vcu, int G, int tid, int wave, int lane) {
;     ...
;         for (int e = 0; e < 8; ++e) lg[e] = wave_sum(lg[e]);
;         int e0 = 0; float b0v = lg[0];
; #pragma unroll
;         for (int e = 1; e < 8; ++e) if (lg[e] > b0v) { b0v = lg[e]; e0 = e; }
;         int e1 = -1; float b1v = -__builtin_inff();
; #pragma unroll
;         for (int e = 0; e < 8; ++e) if (e != e0 && lg[e] > b1v) { b1v = lg[e]; e1 = e; }
;         const float g1 = 1.0f / (1.0f + __expf(b0v - b1v)), g0 = 1.0f - g1;
;         if (lane == 0) {
;             const unsigned k0 = __hip_atomic_fetch_add(lcnt + e0, 1u, __ATOMIC_RELAXED, __HIP_MEMORY_SCOPE_WORKGROUP);
;             const unsigned k1 = __hip_atomic_fetch_add(lcnt + e1, 1u, __ATOMIC_RELAXED, __HIP_MEMORY_SCOPE_WORKGROUP);
;             rinfo[li * 4 + 0] = (unsigned)e0 | ((unsigned)e1 << 8); rinfo[li * 4 + 1] = k0; rinfo[li * 4 + 2] = k1;
;             P.sel_g[2 * m] = g0; P.sel_g[2 * m + 1] = g1;
;         }
;     }
;     LDS_WAIT(); __syncthreads();
;     if (tid < 8) lcnt[8 + tid] = __hip_atomic_fetch_add(P.ctl + CW_CNT + 64 * tid, lcnt[tid], RLX_AGENT);
	v_add_f32_e32 v2, v2, v4
	s_waitcnt lgkmcnt(5)
	v_add_f32_e32 v6, v6, v7
	s_waitcnt lgkmcnt(4)
	v_add_f32_e32 v8, v8, v9
	s_waitcnt lgkmcnt(3)
	v_add_f32_e32 v10, v10, v11
	s_waitcnt lgkmcnt(2)
	v_add_f32_e32 v12, v12, v13
	s_waitcnt lgkmcnt(1)
	v_add_f32_e32 v14, v14, v15
	s_waitcnt lgkmcnt(0)
	v_add_f32_e32 v16, v16, v17
	ds_swizzle_b32 v4, v2 offset:swizzle(SWAP,16)
	ds_swizzle_b32 v7, v6 offset:swizzle(SWAP,16)
	ds_swizzle_b32 v9, v8 offset:swizzle(SWAP,16)
	ds_swizzle_b32 v11, v10 offset:swizzle(SWAP,16)
	ds_swizzle_b32 v13, v12 offset:swizzle(SWAP,16)
	ds_swizzle_b32 v15, v14 offset:swizzle(SWAP,16)
	ds_swizzle_b32 v17, v16 offset:swizzle(SWAP,16)
	s_waitcnt lgkmcnt(6)
	v_add_f32_e32 v2, v2, v4
	s_waitcnt lgkmcnt(5)
	v_add_f32_e32 v6, v6, v7
	s_waitcnt lgkmcnt(4)
	v_add_f32_e32 v8, v8, v9
	s_waitcnt lgkmcnt(3)
	v_add_f32_e32 v10, v10, v11
	s_waitcnt lgkmcnt(2)
	v_add_f32_e32 v12, v12, v13
	s_waitcnt lgkmcnt(1)
	v_add_f32_e32 v14, v14, v15
	s_waitcnt lgkmcnt(0)
	v_add_f32_e32 v16, v16, v17
	v_mov_b32_e32 v5, v3
	v_mov_b32_e32 v4, v2
	v_mov_b32_e32 v7, v6
	v_mov_b32_e32 v9, v8
	v_mov_b32_e32 v11, v10
	v_mov_b32_e32 v13, v12
	v_mov_b32_e32 v15, v14
	v_mov_b32_e32 v17, v16
	v_permlane32_swap_b32_e32 v3, v5
	v_permlane32_swap_b32_e32 v2, v4
	v_permlane32_swap_b32_e32 v6, v7
	v_permlane32_swap_b32_e32 v8, v9
	v_permlane32_swap_b32_e32 v10, v11
	v_permlane32_swap_b32_e32 v12, v13
	v_permlane32_swap_b32_e32 v14, v15
	v_permlane32_swap_b32_e32 v16, v17
	s_and_saveexec_b64 s[28:29], s[38:39]
	s_cbranch_execz .LBB0_1474
	v_pk_add_f32 v[2:3], v[2:3], v[4:5]
	v_add_f32_e32 v6, v6, v7
	v_cmp_gt_f32_e32 vcc, v2, v3
	v_add_f32_e32 v8, v8, v9
	v_add_f32_e32 v10, v10, v11
	v_cndmask_b32_e32 v4, v3, v2, vcc
	v_cmp_gt_f32_e64 s[40:41], v6, v4
	v_add_f32_e32 v12, v12, v13
	v_cndmask_b32_e64 v5, 0, 1, vcc
	v_cndmask_b32_e64 v4, v4, v6, s[40:41]
	v_cmp_gt_f32_e64 s[42:43], v8, v4
	v_cndmask_b32_e64 v5, v5, 2, s[40:41]
	v_add_f32_e32 v14, v14, v15
	v_cndmask_b32_e64 v4, v4, v8, s[42:43]
	v_cmp_gt_f32_e64 s[44:45], v10, v4
	v_cndmask_b32_e64 v5, v5, 3, s[42:43]
	v_add_f32_e32 v16, v16, v17
	v_cndmask_b32_e64 v4, v4, v10, s[44:45]
	v_cmp_gt_f32_e64 s[46:47], v12, v4
	v_cndmask_b32_e64 v5, v5, 4, s[44:45]
	s_mov_b32 s27, 0xff800000
	v_cndmask_b32_e64 v4, v4, v12, s[46:47]
	v_cmp_gt_f32_e64 s[48:49], v14, v4
	v_cndmask_b32_e64 v5, v5, 5, s[46:47]
	v_cmp_nlg_f32_e64 s[52:53], s27, v3
	v_cndmask_b32_e64 v4, v4, v14, s[48:49]
	v_cndmask_b32_e64 v5, v5, 6, s[48:49]
	v_cmp_ngt_f32_e32 vcc, v16, v4
	s_and_b64 s[34:35], s[48:49], vcc
	s_ashr_i32 s27, s26, 31
	v_cndmask_b32_e32 v5, 7, v5, vcc
	v_cmp_eq_u32_e64 s[50:51], 0, v5
	s_or_b64 s[50:51], s[50:51], s[52:53]
	v_cmp_ne_u32_e64 s[48:49], 1, v5
	v_cndmask_b32_e64 v3, v3, v206, s[50:51]
	v_cmp_gt_f32_e64 s[52:53], v2, v3
	s_and_b64 s[48:49], s[48:49], s[52:53]
	v_cndmask_b32_e64 v2, v3, v2, s[48:49]
	v_cmp_ne_u32_e64 s[46:47], 2, v5
	v_cmp_gt_f32_e64 s[52:53], v6, v2
	s_and_b64 s[46:47], s[46:47], s[52:53]
	v_cndmask_b32_e64 v2, v2, v6, s[46:47]
	v_cmp_ne_u32_e64 s[44:45], 3, v5
	v_cmp_gt_f32_e64 s[52:53], v8, v2
	s_and_b64 s[44:45], s[44:45], s[52:53]
	v_cndmask_b32_e64 v2, v2, v8, s[44:45]
	v_cmp_ne_u32_e64 s[42:43], 4, v5
	v_cmp_gt_f32_e64 s[52:53], v10, v2
	s_and_b64 s[42:43], s[42:43], s[52:53]
	v_cndmask_b32_e64 v2, v2, v10, s[42:43]
	v_cmp_ne_u32_e64 s[40:41], 5, v5
	v_cmp_gt_f32_e64 s[52:53], v12, v2
	s_and_b64 s[40:41], s[40:41], s[52:53]
	v_cndmask_b32_e64 v2, v2, v12, s[40:41]
	v_cmp_ngt_f32_e64 s[52:53], v14, v2
	s_or_b64 s[52:53], s[34:35], s[52:53]
	v_cndmask_b32_e32 v4, v16, v4, vcc
	v_cndmask_b32_e64 v2, v14, v2, s[52:53]
	v_cmp_gt_f32_e64 s[54:55], v16, v2
	s_and_b64 s[54:55], vcc, s[54:55]
	v_cndmask_b32_e64 v3, 0, -1, s[50:51]
	v_cndmask_b32_e64 v2, v2, v16, s[54:55]
	v_sub_f32_e32 v2, v4, v2
	v_mul_f32_e32 v2, 0x3fb8aa3b, v2
	v_exp_f32_e32 v2, v2
	v_cndmask_b32_e64 v3, v3, 1, s[48:49]
	v_cndmask_b32_e64 v3, v3, 2, s[46:47]
	v_cndmask_b32_e64 v3, v3, 3, s[44:45]
	v_add_f32_e32 v2, 1.0, v2
	v_div_scale_f32 v4, s[34:35], v2, v2, 1.0
	v_rcp_f32_e32 v6, v4
	v_cndmask_b32_e64 v3, v3, 4, s[42:43]
	v_cndmask_b32_e64 v3, v3, 5, s[40:41]
	v_cndmask_b32_e64 v3, 6, v3, s[52:53]
	v_cndmask_b32_e64 v8, v3, 7, s[54:55]
	v_fma_f32 v3, -v4, v6, 1.0
	v_fmac_f32_e32 v6, v3, v6
	v_div_scale_f32 v3, vcc, 1.0, v2, 1.0
	v_mul_f32_e32 v7, v3, v6
	v_fma_f32 v9, -v4, v7, v3
	v_fmac_f32_e32 v7, v9, v6
	v_fma_f32 v3, -v4, v7, v3
	v_div_fmas_f32 v6, v3, v6, v7
	v_lshl_add_u32 v3, v5, 2, 0
	v_mov_b32_e32 v7, 1
	ds_add_rtn_u32 v3, v3, v7
	v_lshl_add_u32 v4, v8, 2, 0
	ds_add_rtn_u32 v4, v4, v7
	s_lshl_b64 s[34:35], s[26:27], 2
	v_readlane_b32 s44, v253, 44
	v_div_fixup_f32 v7, v6, v2, 1.0
	s_add_u32 s34, s18, s34
	v_readlane_b32 s53, v254, 43
	v_readlane_b32 s45, v253, 45
	v_readlane_b32 s50, v254, 40
	v_readlane_b32 s48, v254, 38
	v_sub_f32_e32 v6, 1.0, v7
	v_lshl_add_u32 v2, v8, 8, v5
	v_mov_b32_e32 v5, s23
	s_addc_u32 s35, s19, s35
	v_readlane_b32 s51, v254, 41
	v_readlane_b32 s49, v254, 39
	s_waitcnt lgkmcnt(0)
	ds_write_b96 v5, v[2:4]
	global_store_dwordx2 v1, v[6:7], s[34:35] sc0 sc1
	s_branch .LBB0_1474
.LBB0_1477:
	s_waitcnt vmcnt(0)
	s_waitcnt lgkmcnt(0)
	v_cmp_gt_i32_e32 vcc, 8, v36
	s_waitcnt lgkmcnt(0)
	s_barrier
	s_and_saveexec_b64 s[18:19], vcc
	s_cbranch_execz .LBB0_1479
	v_lshlrev_b32_e32 v2, 6, v36
	ds_read_b32 v4, v0
	v_ashrrev_i32_e32 v3, 31, v2
	v_lshl_add_u64 v[2:3], v[2:3], 2, s[16:17]
	v_add_co_u32_e32 v2, vcc, 0x8000, v2
	s_nop 1
	v_addc_co_u32_e32 v3, vcc, 0, v3, vcc
	s_waitcnt lgkmcnt(0)
	global_atomic_add v2, v[2:3], v4, off offset:1024 sc0
	s_waitcnt vmcnt(0)
	ds_write_b32 v0, v2 offset:32
